# speedup vs baseline: 1.0247x; 1.0247x over previous
.Lq_go_3:
	ds_read_b128 v[228:231], v5 offset:49152
	ds_read_b128 v[232:235], v5 offset:49664
	ds_read_b128 v[236:239], v5 offset:50176
	ds_read_b128 v[240:243], v5 offset:50688
	v_mul_f32_e32 v244, v212, v216
	v_mul_f32_e32 v250, v213, v217
	v_mul_f32_e64 v245, -v216, v216
	v_mul_f32_e64 v251, -v217, v217
	v_add_f32_e32 v246, v212, v216
	v_add_f32_e32 v252, v213, v217
	v_fma_f32 v245, -v212, v212, v245
	v_fma_f32 v251, -v213, v213, v251
	v_fma_f32 v247, v10, v246, v11
	v_fma_f32 v253, v10, v252, v11
	v_fma_f32 v246, v13, v224, v14
	v_fma_f32 v252, v13, v225, v14
	v_fma_f32 v248, v12, v220, v245
	v_fma_f32 v254, v12, v221, v251
	v_fma_f32 v249, 2.0, v244, v247
	v_fma_f32 v255, 2.0, v250, v253
	v_sub_f32_e32 v247, v247, v245
	v_sub_f32_e32 v253, v253, v251
	v_fma_f32 v246, -2.0, v244, v246
	v_fma_f32 v252, -2.0, v250, v252
	v_mul_f32_e32 v247, v247, v248
	v_mul_f32_e32 v253, v253, v254
	v_rcp_f32_e32 v247, v247
	v_rcp_f32_e32 v253, v253
	v_mul_f32_e32 v249, v249, v246
	v_mul_f32_e32 v255, v255, v252
	v_fma_f32 v21, v249, v247, v21
	v_fma_f32 v21, v255, v253, v21
	v_mul_f32_e32 v244, v214, v218
	v_mul_f32_e32 v250, v215, v219
	v_mul_f32_e64 v245, -v218, v218
	v_mul_f32_e64 v251, -v219, v219
	v_add_f32_e32 v246, v214, v218
	v_add_f32_e32 v252, v215, v219
	v_fma_f32 v245, -v214, v214, v245
	v_fma_f32 v251, -v215, v215, v251
	v_fma_f32 v247, v10, v246, v11
	v_fma_f32 v253, v10, v252, v11
	v_fma_f32 v246, v13, v226, v14
	v_fma_f32 v252, v13, v227, v14
	v_fma_f32 v248, v12, v222, v245
	v_fma_f32 v254, v12, v223, v251
	v_fma_f32 v249, 2.0, v244, v247
	v_fma_f32 v255, 2.0, v250, v253
	v_sub_f32_e32 v247, v247, v245
	v_sub_f32_e32 v253, v253, v251
	v_fma_f32 v246, -2.0, v244, v246
	v_fma_f32 v252, -2.0, v250, v252
	v_mul_f32_e32 v247, v247, v248
	v_mul_f32_e32 v253, v253, v254
	v_rcp_f32_e32 v247, v247
	v_rcp_f32_e32 v253, v253
	v_mul_f32_e32 v249, v249, v246
	v_mul_f32_e32 v255, v255, v252
	v_fma_f32 v22, v249, v247, v22
	v_fma_f32 v22, v255, v253, v22
	s_waitcnt lgkmcnt(0)
	v_mfma_f32_16x16x32_f16 v[212:215], v[28:31], v[228:231], 0
	v_mfma_f32_16x16x32_f16 v[216:219], v[28:31], v[232:235], 0
	v_mfma_f32_16x16x32_f16 v[220:223], v[28:31], v[236:239], v[0:3]
	v_mfma_f32_16x16x32_f16 v[224:227], v[28:31], v[240:243], 0
	v_mfma_f32_16x16x32_f16 v[212:215], v[32:35], v[164:167], v[212:215]
	v_mfma_f32_16x16x32_f16 v[216:219], v[32:35], v[172:175], v[216:219]
	v_mfma_f32_16x16x32_f16 v[220:223], v[32:35], v[180:183], v[220:223]
	v_mfma_f32_16x16x32_f16 v[224:227], v[32:35], v[188:191], v[224:227]
	v_mul_f32_e32 v244, v196, v200
	v_mul_f32_e32 v250, v197, v201
	v_mul_f32_e64 v245, -v200, v200
	v_mul_f32_e64 v251, -v201, v201
	v_add_f32_e32 v246, v196, v200
	v_add_f32_e32 v252, v197, v201
	v_fma_f32 v245, -v196, v196, v245
	v_fma_f32 v251, -v197, v197, v251
	v_fma_f32 v247, v10, v246, v11
	v_fma_f32 v253, v10, v252, v11
	v_fma_f32 v246, v13, v208, v14
	v_fma_f32 v252, v13, v209, v14
	v_fma_f32 v248, v12, v204, v245
	v_fma_f32 v254, v12, v205, v251
	v_fma_f32 v249, 2.0, v244, v247
	v_fma_f32 v255, 2.0, v250, v253
	v_sub_f32_e32 v247, v247, v245
	v_sub_f32_e32 v253, v253, v251
	v_fma_f32 v246, -2.0, v244, v246
	v_fma_f32 v252, -2.0, v250, v252
	v_mul_f32_e32 v247, v247, v248
	v_mul_f32_e32 v253, v253, v254
	v_rcp_f32_e32 v247, v247
	v_rcp_f32_e32 v253, v253
	v_mul_f32_e32 v249, v249, v246
	v_mul_f32_e32 v255, v255, v252
	v_fma_f32 v21, v249, v247, v21
	v_fma_f32 v21, v255, v253, v21
	v_mul_f32_e32 v244, v198, v202
	v_mul_f32_e32 v250, v199, v203
	v_mul_f32_e64 v245, -v202, v202
	v_mul_f32_e64 v251, -v203, v203
	v_add_f32_e32 v246, v198, v202
	v_add_f32_e32 v252, v199, v203
	v_fma_f32 v245, -v198, v198, v245
	v_fma_f32 v251, -v199, v199, v251
	v_fma_f32 v247, v10, v246, v11
	v_fma_f32 v253, v10, v252, v11
	v_fma_f32 v246, v13, v210, v14
	v_fma_f32 v252, v13, v211, v14
	v_fma_f32 v248, v12, v206, v245
	v_fma_f32 v254, v12, v207, v251
	v_fma_f32 v249, 2.0, v244, v247
	v_fma_f32 v255, 2.0, v250, v253
	v_sub_f32_e32 v247, v247, v245
	v_sub_f32_e32 v253, v253, v251
	v_fma_f32 v246, -2.0, v244, v246
	v_fma_f32 v252, -2.0, v250, v252
	v_mul_f32_e32 v247, v247, v248
	v_mul_f32_e32 v253, v253, v254
	v_rcp_f32_e32 v247, v247
	v_rcp_f32_e32 v253, v253
	v_mul_f32_e32 v249, v249, v246
	v_mul_f32_e32 v255, v255, v252
	v_fma_f32 v22, v249, v247, v22
	v_fma_f32 v22, v255, v253, v22
	v_mul_f32_e32 v244, v212, v216
	v_mul_f32_e32 v250, v213, v217
	v_mul_f32_e64 v245, -v216, v216
	v_mul_f32_e64 v251, -v217, v217
	v_add_f32_e32 v246, v212, v216
	v_add_f32_e32 v252, v213, v217
	v_fma_f32 v245, -v212, v212, v245
	v_fma_f32 v251, -v213, v213, v251
	v_fma_f32 v247, v10, v246, v11
	v_fma_f32 v253, v10, v252, v11
	v_fma_f32 v246, v13, v224, v14
	v_fma_f32 v252, v13, v225, v14
	v_fma_f32 v248, v12, v220, v245
	v_fma_f32 v254, v12, v221, v251
	v_fma_f32 v249, 2.0, v244, v247
	v_fma_f32 v255, 2.0, v250, v253
	v_sub_f32_e32 v247, v247, v245
	v_sub_f32_e32 v253, v253, v251
	v_fma_f32 v246, -2.0, v244, v246
	v_fma_f32 v252, -2.0, v250, v252
	v_mul_f32_e32 v247, v247, v248
	v_mul_f32_e32 v253, v253, v254
	v_rcp_f32_e32 v247, v247
	v_rcp_f32_e32 v253, v253
	v_mul_f32_e32 v249, v249, v246
	v_mul_f32_e32 v255, v255, v252
	v_mul_f32_e32 v249, v249, v247
	v_mul_f32_e32 v255, v255, v253
	v_fma_f32 v21, v249, v15, v21
	v_fma_f32 v21, v255, v16, v21
	v_mul_f32_e32 v244, v214, v218
	v_mul_f32_e32 v250, v215, v219
	v_mul_f32_e64 v245, -v218, v218
	v_mul_f32_e64 v251, -v219, v219
	v_add_f32_e32 v246, v214, v218
	v_add_f32_e32 v252, v215, v219
	v_fma_f32 v245, -v214, v214, v245
	v_fma_f32 v251, -v215, v215, v251
	v_fma_f32 v247, v10, v246, v11
	v_fma_f32 v253, v10, v252, v11
	v_fma_f32 v246, v13, v226, v14
	v_fma_f32 v252, v13, v227, v14
	v_fma_f32 v248, v12, v222, v245
	v_fma_f32 v254, v12, v223, v251
	v_fma_f32 v249, 2.0, v244, v247
	v_fma_f32 v255, 2.0, v250, v253
	v_sub_f32_e32 v247, v247, v245
	v_sub_f32_e32 v253, v253, v251
	v_fma_f32 v246, -2.0, v244, v246
	v_fma_f32 v252, -2.0, v250, v252
	v_mul_f32_e32 v247, v247, v248
	v_mul_f32_e32 v253, v253, v254
	v_rcp_f32_e32 v247, v247
	v_rcp_f32_e32 v253, v253
	v_mul_f32_e32 v249, v249, v246
	v_mul_f32_e32 v255, v255, v252
	v_mul_f32_e32 v249, v249, v247
	v_mul_f32_e32 v255, v255, v253
	v_fma_f32 v22, v249, v17, v22
	v_fma_f32 v22, v255, v18, v22
	v_add_f32_e32 v19, v19, v20
	v_add_f32_e32 v21, v21, v22
	v_and_b32_e32 v23, 15, v8
	s_cmp_eq_u32 s15, 7
	s_cselect_b32 s23, 6, 16
	v_cmp_gt_u32_e32 vcc, s23, v23
	s_nop 1
	v_cndmask_b32_e32 v21, 0, v21, vcc
	v_add_f32_e32 v19, v19, v21
	s_nop 1
	v_add_f32_dpp v19, v19, v19 quad_perm:[1,0,3,2] row_mask:0xf bank_mask:0xf
	s_nop 1
	v_add_f32_dpp v19, v19, v19 quad_perm:[2,3,0,1] row_mask:0xf bank_mask:0xf
	s_nop 1
	v_add_f32_dpp v19, v19, v19 row_half_mirror row_mask:0xf bank_mask:0xf
	s_nop 1
	v_add_f32_dpp v19, v19, v19 row_mirror row_mask:0xf bank_mask:0xf
	s_nop 0
	v_readlane_b32 s40, v19, 0
	v_readlane_b32 s41, v19, 16
	v_readlane_b32 s42, v19, 32
	v_readlane_b32 s43, v19, 48
	s_lshl_b32 s24, s2, 3
	s_add_u32 s24, s24, s12
	s_lshl_b32 s24, s24, 2
	v_mov_b32_e32 v19, s40
	v_add_f32_e32 v19, s41, v19
	v_add_f32_e32 v19, s42, v19
	v_add_f32_e32 v19, s43, v19
	v_mov_b32_e32 v9, s24
	v_cmp_eq_u32_e32 vcc, 0, v8
	s_nop 1
	s_and_saveexec_b64 s[30:31], vcc
	global_store_dword v9, v19, s[10:11] sc0 sc1
	s_endpgm
